# removed mid-phase s_setprio 0/1 flip pairs in the four GEMM K-loops
# speedup vs baseline: 1.0065x; 1.0001x over previous
.LBB0_157:
	ds_read_b128 v[150:153], v163
	ds_read_b128 v[154:157], v164
	ds_read_b128 v[178:181], v158
	ds_read_b128 v[182:185], v159
	ds_read_b128 v[186:189], v165
	ds_read_b128 v[190:193], v166
	ds_read_b128 v[194:197], v167
	ds_read_b128 v[198:201], v168
	s_add_u32 s44, s42, 0x80
	s_addc_u32 s45, s43, 0
	s_cmp_eq_u32 s73, 28
	s_cselect_b32 s47, s31, s45
	s_cselect_b32 s46, s39, s44
	s_cselect_b32 s45, s29, s72
	s_cselect_b32 s44, s70, s71
	v_lshl_add_u64 v[234:235], s[42:43], 0, v[142:143]
	s_add_i32 m0, s21, 0xc000
	ds_read_b128 v[202:205], v176
	ds_read_b128 v[206:209], v176 offset:1024
	ds_read_b128 v[210:213], v176 offset:2048
	ds_read_b128 v[214:217], v176 offset:3072
	ds_read_b128 v[218:221], v176 offset:4096
	ds_read_b128 v[222:225], v176 offset:5120
	ds_read_b128 v[226:229], v176 offset:6144
	ds_read_b128 v[230:233], v176 offset:7168
	global_load_lds_dwordx4 v[234:235], off
	v_lshl_add_u64 v[234:235], s[42:43], 0, v[144:145]
	s_add_i32 m0, s21, 0xe000
	s_nop 0
	global_load_lds_dwordx4 v[234:235], off
	s_waitcnt vmcnt(8)
	s_waitcnt lgkmcnt(0)
	s_barrier
	s_setprio 1
	s_waitcnt lgkmcnt(0)
	v_mfma_f32_16x16x32_bf16 v[126:129], v[178:181], v[202:205], v[126:129]
	v_mfma_f32_16x16x32_bf16 v[122:125], v[154:157], v[202:205], v[122:125]
	v_mfma_f32_16x16x32_bf16 v[110:113], v[178:181], v[210:213], v[110:113]
	v_mfma_f32_16x16x32_bf16 v[106:109], v[154:157], v[210:213], v[106:109]
	v_mfma_f32_16x16x32_bf16 v[94:97], v[178:181], v[218:221], v[94:97]
	v_mfma_f32_16x16x32_bf16 v[90:93], v[154:157], v[218:221], v[90:93]
	v_mfma_f32_16x16x32_bf16 v[78:81], v[178:181], v[226:229], v[78:81]
	v_mfma_f32_16x16x32_bf16 v[74:77], v[154:157], v[226:229], v[74:77]
	v_mfma_f32_16x16x32_bf16 v[126:129], v[150:153], v[206:209], v[126:129]
	v_mfma_f32_16x16x32_bf16 v[122:125], v[186:189], v[206:209], v[122:125]
	v_mfma_f32_16x16x32_bf16 v[110:113], v[150:153], v[214:217], v[110:113]
	v_mfma_f32_16x16x32_bf16 v[106:109], v[186:189], v[214:217], v[106:109]
	v_mfma_f32_16x16x32_bf16 v[94:97], v[150:153], v[222:225], v[94:97]
	v_mfma_f32_16x16x32_bf16 v[90:93], v[186:189], v[222:225], v[90:93]
	v_mfma_f32_16x16x32_bf16 v[78:81], v[150:153], v[230:233], v[78:81]
	v_mfma_f32_16x16x32_bf16 v[74:77], v[186:189], v[230:233], v[74:77]
	v_mfma_f32_16x16x32_bf16 v[118:121], v[182:185], v[202:205], v[118:121]
	v_mfma_f32_16x16x32_bf16 v[114:117], v[194:197], v[202:205], v[114:117]
	v_mfma_f32_16x16x32_bf16 v[102:105], v[182:185], v[210:213], v[102:105]
	v_mfma_f32_16x16x32_bf16 v[98:101], v[194:197], v[210:213], v[98:101]
	v_mfma_f32_16x16x32_bf16 v[86:89], v[182:185], v[218:221], v[86:89]
	v_mfma_f32_16x16x32_bf16 v[82:85], v[194:197], v[218:221], v[82:85]
	v_mfma_f32_16x16x32_bf16 v[70:73], v[182:185], v[226:229], v[70:73]
	v_mfma_f32_16x16x32_bf16 v[66:69], v[194:197], v[226:229], v[66:69]
	v_mfma_f32_16x16x32_bf16 v[118:121], v[190:193], v[206:209], v[118:121]
	v_mfma_f32_16x16x32_bf16 v[114:117], v[198:201], v[206:209], v[114:117]
	v_mfma_f32_16x16x32_bf16 v[102:105], v[190:193], v[214:217], v[102:105]
	v_mfma_f32_16x16x32_bf16 v[98:101], v[198:201], v[214:217], v[98:101]
	v_mfma_f32_16x16x32_bf16 v[86:89], v[190:193], v[222:225], v[86:89]
	v_mfma_f32_16x16x32_bf16 v[82:85], v[198:201], v[222:225], v[82:85]
	v_mfma_f32_16x16x32_bf16 v[70:73], v[190:193], v[230:233], v[70:73]
	v_mfma_f32_16x16x32_bf16 v[66:69], v[198:201], v[230:233], v[66:69]
	s_setprio 0
	s_barrier
	s_mov_b32 m0, s23
	v_lshl_add_u64 v[234:235], s[44:45], 0, v[130:131]
	s_add_u32 s74, s44, 0x80000
	ds_read_b128 v[202:205], v176 offset:16384
	ds_read_b128 v[206:209], v176 offset:17408
	ds_read_b128 v[210:213], v176 offset:18432
	ds_read_b128 v[214:217], v176 offset:19456
	ds_read_b128 v[218:221], v176 offset:20480
	ds_read_b128 v[222:225], v176 offset:21504
	ds_read_b128 v[226:229], v176 offset:22528
	ds_read_b128 v[230:233], v176 offset:23552
	global_load_lds_dwordx4 v[234:235], off
	v_lshl_add_u64 v[236:237], s[44:45], 0, v[136:137]
	s_mov_b32 m0, s25
	s_addc_u32 s75, s45, 0
	global_load_lds_dwordx4 v[236:237], off
	v_lshl_add_u64 v[238:239], s[74:75], 0, v[130:131]
	s_mov_b32 m0, s27
	v_lshl_add_u64 v[240:241], s[46:47], 0, v[138:139]
	global_load_lds_dwordx4 v[238:239], off
	v_lshl_add_u64 v[238:239], s[74:75], 0, v[136:137]
	s_mov_b32 m0, s33
	s_nop 0
	global_load_lds_dwordx4 v[238:239], off
	v_lshl_add_u64 v[238:239], s[46:47], 0, v[132:133]
	s_mov_b32 m0, s21
	s_nop 0
	global_load_lds_dwordx4 v[238:239], off
	s_mov_b32 m0, s41
	s_nop 0
	global_load_lds_dwordx4 v[240:241], off
	s_waitcnt vmcnt(8)
	s_waitcnt lgkmcnt(0)
	s_barrier
	s_setprio 1
	s_waitcnt lgkmcnt(0)
	v_mfma_f32_16x16x32_bf16 v[62:65], v[178:181], v[202:205], v[62:65]
	v_mfma_f32_16x16x32_bf16 v[58:61], v[154:157], v[202:205], v[58:61]
	v_mfma_f32_16x16x32_bf16 v[46:49], v[178:181], v[210:213], v[46:49]
	v_mfma_f32_16x16x32_bf16 v[42:45], v[154:157], v[210:213], v[42:45]
	v_mfma_f32_16x16x32_bf16 v[30:33], v[178:181], v[218:221], v[30:33]
	v_mfma_f32_16x16x32_bf16 v[26:29], v[154:157], v[218:221], v[26:29]
	v_mfma_f32_16x16x32_bf16 v[14:17], v[178:181], v[226:229], v[14:17]
	v_mfma_f32_16x16x32_bf16 v[10:13], v[154:157], v[226:229], v[10:13]
	v_mfma_f32_16x16x32_bf16 v[62:65], v[150:153], v[206:209], v[62:65]
	v_mfma_f32_16x16x32_bf16 v[58:61], v[186:189], v[206:209], v[58:61]
	v_mfma_f32_16x16x32_bf16 v[46:49], v[150:153], v[214:217], v[46:49]
	v_mfma_f32_16x16x32_bf16 v[42:45], v[186:189], v[214:217], v[42:45]
	v_mfma_f32_16x16x32_bf16 v[30:33], v[150:153], v[222:225], v[30:33]
	v_mfma_f32_16x16x32_bf16 v[26:29], v[186:189], v[222:225], v[26:29]
	v_mfma_f32_16x16x32_bf16 v[14:17], v[150:153], v[230:233], v[14:17]
	v_mfma_f32_16x16x32_bf16 v[10:13], v[186:189], v[230:233], v[10:13]
	v_mfma_f32_16x16x32_bf16 v[54:57], v[182:185], v[202:205], v[54:57]
	v_mfma_f32_16x16x32_bf16 v[50:53], v[194:197], v[202:205], v[50:53]
	v_mfma_f32_16x16x32_bf16 v[38:41], v[182:185], v[210:213], v[38:41]
	v_mfma_f32_16x16x32_bf16 v[34:37], v[194:197], v[210:213], v[34:37]
	v_mfma_f32_16x16x32_bf16 v[18:21], v[182:185], v[218:221], v[18:21]
	v_mfma_f32_16x16x32_bf16 v[22:25], v[194:197], v[218:221], v[22:25]
	v_mfma_f32_16x16x32_bf16 v[2:5], v[182:185], v[226:229], v[2:5]
	v_mfma_f32_16x16x32_bf16 v[6:9], v[194:197], v[226:229], v[6:9]
	v_mfma_f32_16x16x32_bf16 v[54:57], v[190:193], v[206:209], v[54:57]
	v_mfma_f32_16x16x32_bf16 v[50:53], v[198:201], v[206:209], v[50:53]
	v_mfma_f32_16x16x32_bf16 v[38:41], v[190:193], v[214:217], v[38:41]
	v_mfma_f32_16x16x32_bf16 v[34:37], v[198:201], v[214:217], v[34:37]
	v_mfma_f32_16x16x32_bf16 v[18:21], v[190:193], v[222:225], v[18:21]
	v_mfma_f32_16x16x32_bf16 v[22:25], v[198:201], v[222:225], v[22:25]
	v_mfma_f32_16x16x32_bf16 v[2:5], v[190:193], v[230:233], v[2:5]
	v_mfma_f32_16x16x32_bf16 v[6:9], v[198:201], v[230:233], v[6:9]
	s_setprio 0
	s_barrier
	ds_read_b128 v[150:153], v169
	ds_read_b128 v[154:157], v170
	ds_read_b128 v[178:181], v160
	ds_read_b128 v[182:185], v161
	ds_read_b128 v[186:189], v171
	ds_read_b128 v[190:193], v172
	ds_read_b128 v[194:197], v173
	ds_read_b128 v[198:201], v174
	s_mov_b32 m0, s53
	v_lshl_add_u64 v[242:243], s[46:47], 0, v[134:135]
	ds_read_b128 v[202:205], v176 offset:32768
	ds_read_b128 v[206:209], v176 offset:33792
	ds_read_b128 v[210:213], v176 offset:34816
	ds_read_b128 v[214:217], v176 offset:35840
	ds_read_b128 v[218:221], v176 offset:36864
	ds_read_b128 v[222:225], v176 offset:37888
	ds_read_b128 v[226:229], v176 offset:38912
	ds_read_b128 v[230:233], v176 offset:39936
	global_load_lds_dwordx4 v[242:243], off
	v_lshl_add_u64 v[242:243], s[46:47], 0, v[140:141]
	s_mov_b32 m0, s55
	s_nop 0
	global_load_lds_dwordx4 v[242:243], off
	s_waitcnt vmcnt(8)
	s_waitcnt lgkmcnt(0)
	s_barrier
	s_setprio 1
	s_waitcnt lgkmcnt(0)
	v_mfma_f32_16x16x32_bf16 v[126:129], v[178:181], v[202:205], v[126:129]
	v_mfma_f32_16x16x32_bf16 v[122:125], v[154:157], v[202:205], v[122:125]
	v_mfma_f32_16x16x32_bf16 v[110:113], v[178:181], v[210:213], v[110:113]
	v_mfma_f32_16x16x32_bf16 v[106:109], v[154:157], v[210:213], v[106:109]
	v_mfma_f32_16x16x32_bf16 v[94:97], v[178:181], v[218:221], v[94:97]
	v_mfma_f32_16x16x32_bf16 v[90:93], v[154:157], v[218:221], v[90:93]
	v_mfma_f32_16x16x32_bf16 v[78:81], v[178:181], v[226:229], v[78:81]
	v_mfma_f32_16x16x32_bf16 v[74:77], v[154:157], v[226:229], v[74:77]
	v_mfma_f32_16x16x32_bf16 v[126:129], v[150:153], v[206:209], v[126:129]
	v_mfma_f32_16x16x32_bf16 v[122:125], v[186:189], v[206:209], v[122:125]
	v_mfma_f32_16x16x32_bf16 v[110:113], v[150:153], v[214:217], v[110:113]
	v_mfma_f32_16x16x32_bf16 v[106:109], v[186:189], v[214:217], v[106:109]
	v_mfma_f32_16x16x32_bf16 v[94:97], v[150:153], v[222:225], v[94:97]
	v_mfma_f32_16x16x32_bf16 v[90:93], v[186:189], v[222:225], v[90:93]
	v_mfma_f32_16x16x32_bf16 v[78:81], v[150:153], v[230:233], v[78:81]
	v_mfma_f32_16x16x32_bf16 v[74:77], v[186:189], v[230:233], v[74:77]
	v_mfma_f32_16x16x32_bf16 v[118:121], v[182:185], v[202:205], v[118:121]
	v_mfma_f32_16x16x32_bf16 v[114:117], v[194:197], v[202:205], v[114:117]
	v_mfma_f32_16x16x32_bf16 v[102:105], v[182:185], v[210:213], v[102:105]
	v_mfma_f32_16x16x32_bf16 v[98:101], v[194:197], v[210:213], v[98:101]
	v_mfma_f32_16x16x32_bf16 v[86:89], v[182:185], v[218:221], v[86:89]
	v_mfma_f32_16x16x32_bf16 v[82:85], v[194:197], v[218:221], v[82:85]
	v_mfma_f32_16x16x32_bf16 v[70:73], v[182:185], v[226:229], v[70:73]
	v_mfma_f32_16x16x32_bf16 v[66:69], v[194:197], v[226:229], v[66:69]
	v_mfma_f32_16x16x32_bf16 v[118:121], v[190:193], v[206:209], v[118:121]
	v_mfma_f32_16x16x32_bf16 v[114:117], v[198:201], v[206:209], v[114:117]
	v_mfma_f32_16x16x32_bf16 v[102:105], v[190:193], v[214:217], v[102:105]
	v_mfma_f32_16x16x32_bf16 v[98:101], v[198:201], v[214:217], v[98:101]
	v_mfma_f32_16x16x32_bf16 v[86:89], v[190:193], v[222:225], v[86:89]
	v_mfma_f32_16x16x32_bf16 v[82:85], v[198:201], v[222:225], v[82:85]
	v_mfma_f32_16x16x32_bf16 v[70:73], v[190:193], v[230:233], v[70:73]
	v_mfma_f32_16x16x32_bf16 v[66:69], v[198:201], v[230:233], v[66:69]
	s_setprio 0
	s_barrier
	s_mov_b32 m0, s60
	v_lshl_add_u64 v[234:235], v[234:235], 0, s[10:11]
	s_add_u32 s44, s44, 0x80080
	ds_read_b128 v[202:205], v176 offset:49152
	ds_read_b128 v[206:209], v176 offset:50176
	ds_read_b128 v[210:213], v176 offset:51200
	ds_read_b128 v[214:217], v176 offset:52224
	ds_read_b128 v[218:221], v176 offset:53248
	ds_read_b128 v[222:225], v176 offset:54272
	ds_read_b128 v[226:229], v176 offset:55296
	ds_read_b128 v[230:233], v176 offset:56320
	global_load_lds_dwordx4 v[234:235], off
	v_lshl_add_u64 v[234:235], v[236:237], 0, s[10:11]
	s_mov_b32 m0, s61
	s_addc_u32 s45, s45, 0
	global_load_lds_dwordx4 v[234:235], off
	v_lshl_add_u64 v[234:235], s[44:45], 0, v[130:131]
	s_mov_b32 m0, s64
	s_nop 0
	global_load_lds_dwordx4 v[234:235], off
	v_lshl_add_u64 v[234:235], s[44:45], 0, v[136:137]
	s_mov_b32 m0, s65
	s_nop 0
	global_load_lds_dwordx4 v[234:235], off
	v_lshl_add_u64 v[234:235], v[238:239], 0, s[10:11]
	s_mov_b32 m0, s62
	s_nop 0
	global_load_lds_dwordx4 v[234:235], off
	v_lshl_add_u64 v[234:235], v[240:241], 0, s[10:11]
	s_mov_b32 m0, s63
	s_nop 0
	global_load_lds_dwordx4 v[234:235], off
	s_waitcnt vmcnt(8)
	s_waitcnt lgkmcnt(0)
	s_barrier
	s_setprio 1
	s_waitcnt lgkmcnt(0)
	v_mfma_f32_16x16x32_bf16 v[62:65], v[178:181], v[202:205], v[62:65]
	v_mfma_f32_16x16x32_bf16 v[58:61], v[154:157], v[202:205], v[58:61]
	v_mfma_f32_16x16x32_bf16 v[46:49], v[178:181], v[210:213], v[46:49]
	v_mfma_f32_16x16x32_bf16 v[42:45], v[154:157], v[210:213], v[42:45]
	v_mfma_f32_16x16x32_bf16 v[30:33], v[178:181], v[218:221], v[30:33]
	v_mfma_f32_16x16x32_bf16 v[26:29], v[154:157], v[218:221], v[26:29]
	v_mfma_f32_16x16x32_bf16 v[14:17], v[178:181], v[226:229], v[14:17]
	v_mfma_f32_16x16x32_bf16 v[10:13], v[154:157], v[226:229], v[10:13]
	v_mfma_f32_16x16x32_bf16 v[62:65], v[150:153], v[206:209], v[62:65]
	v_mfma_f32_16x16x32_bf16 v[58:61], v[186:189], v[206:209], v[58:61]
	v_mfma_f32_16x16x32_bf16 v[46:49], v[150:153], v[214:217], v[46:49]
	v_mfma_f32_16x16x32_bf16 v[42:45], v[186:189], v[214:217], v[42:45]
	v_mfma_f32_16x16x32_bf16 v[30:33], v[150:153], v[222:225], v[30:33]
	v_mfma_f32_16x16x32_bf16 v[26:29], v[186:189], v[222:225], v[26:29]
	v_mfma_f32_16x16x32_bf16 v[14:17], v[150:153], v[230:233], v[14:17]
	v_mfma_f32_16x16x32_bf16 v[10:13], v[186:189], v[230:233], v[10:13]
	v_mfma_f32_16x16x32_bf16 v[54:57], v[182:185], v[202:205], v[54:57]
	v_mfma_f32_16x16x32_bf16 v[50:53], v[194:197], v[202:205], v[50:53]
	v_mfma_f32_16x16x32_bf16 v[38:41], v[182:185], v[210:213], v[38:41]
	v_mfma_f32_16x16x32_bf16 v[34:37], v[194:197], v[210:213], v[34:37]
	v_mfma_f32_16x16x32_bf16 v[18:21], v[182:185], v[218:221], v[18:21]
	v_mfma_f32_16x16x32_bf16 v[22:25], v[194:197], v[218:221], v[22:25]
	v_mfma_f32_16x16x32_bf16 v[2:5], v[182:185], v[226:229], v[2:5]
	v_mfma_f32_16x16x32_bf16 v[6:9], v[194:197], v[226:229], v[6:9]
	v_mfma_f32_16x16x32_bf16 v[54:57], v[190:193], v[206:209], v[54:57]
	v_mfma_f32_16x16x32_bf16 v[50:53], v[198:201], v[206:209], v[50:53]
	v_mfma_f32_16x16x32_bf16 v[38:41], v[190:193], v[214:217], v[38:41]
	v_mfma_f32_16x16x32_bf16 v[34:37], v[198:201], v[214:217], v[34:37]
	v_mfma_f32_16x16x32_bf16 v[18:21], v[190:193], v[222:225], v[18:21]
	v_mfma_f32_16x16x32_bf16 v[22:25], v[198:201], v[222:225], v[22:25]
	v_mfma_f32_16x16x32_bf16 v[2:5], v[190:193], v[230:233], v[2:5]
	v_mfma_f32_16x16x32_bf16 v[6:9], v[198:201], v[230:233], v[6:9]
	s_setprio 0
	s_barrier
	s_add_i32 s73, s73, 2
	s_add_u32 s42, s42, 0x100
	s_addc_u32 s43, s43, 0
	s_add_u32 s71, s71, 0x100
	s_addc_u32 s72, s72, 0
	s_cmp_gt_u32 s73, 29
	s_cbranch_scc0 .LBB0_157
	s_and_b64 vcc, exec, s[12:13]
	s_cbranch_vccz .LBB0_160
	s_barrier

.LBB0_534:
	ds_read_b128 v[172:175], v156
	ds_read_b128 v[176:179], v157
	ds_read_b128 v[180:183], v152
	ds_read_b128 v[184:187], v153
	ds_read_b128 v[188:191], v158
	ds_read_b128 v[192:195], v159
	ds_read_b128 v[196:199], v160
	ds_read_b128 v[200:203], v161
	s_add_u32 s36, s34, 0x80
	s_addc_u32 s37, s35, 0
	s_cmp_eq_u32 s74, 28
	s_cselect_b32 s39, s25, s37
	s_cselect_b32 s38, s70, s36
	s_cselect_b32 s37, s23, s73
	s_cselect_b32 s36, s71, s72
	v_lshl_add_u64 v[150:151], s[34:35], 0, v[142:143]
	s_add_i32 m0, s31, 0xc000
	ds_read_b128 v[204:207], v170
	ds_read_b128 v[208:211], v170 offset:1024
	ds_read_b128 v[212:215], v170 offset:2048
	ds_read_b128 v[216:219], v170 offset:3072
	ds_read_b128 v[220:223], v170 offset:4096
	ds_read_b128 v[224:227], v170 offset:5120
	ds_read_b128 v[228:231], v170 offset:6144
	ds_read_b128 v[232:235], v170 offset:7168
	global_load_lds_dwordx4 v[150:151], off
	v_lshl_add_u64 v[150:151], s[34:35], 0, v[144:145]
	s_add_i32 m0, s31, 0xe000
	s_nop 0
	global_load_lds_dwordx4 v[150:151], off
	s_waitcnt vmcnt(8)
	s_waitcnt lgkmcnt(0)
	s_barrier
	s_setprio 1
	s_waitcnt lgkmcnt(0)
	v_mfma_f32_16x16x32_bf16 v[126:129], v[180:183], v[204:207], v[126:129]
	v_mfma_f32_16x16x32_bf16 v[122:125], v[176:179], v[204:207], v[122:125]
	v_mfma_f32_16x16x32_bf16 v[118:121], v[180:183], v[212:215], v[118:121]
	v_mfma_f32_16x16x32_bf16 v[110:113], v[176:179], v[212:215], v[110:113]
	v_mfma_f32_16x16x32_bf16 v[102:105], v[180:183], v[220:223], v[102:105]
	v_mfma_f32_16x16x32_bf16 v[94:97], v[176:179], v[220:223], v[94:97]
	v_mfma_f32_16x16x32_bf16 v[86:89], v[180:183], v[228:231], v[86:89]
	v_mfma_f32_16x16x32_bf16 v[78:81], v[176:179], v[228:231], v[78:81]
	v_mfma_f32_16x16x32_bf16 v[126:129], v[172:175], v[208:211], v[126:129]
	v_mfma_f32_16x16x32_bf16 v[122:125], v[188:191], v[208:211], v[122:125]
	v_mfma_f32_16x16x32_bf16 v[118:121], v[172:175], v[216:219], v[118:121]
	v_mfma_f32_16x16x32_bf16 v[110:113], v[188:191], v[216:219], v[110:113]
	v_mfma_f32_16x16x32_bf16 v[102:105], v[172:175], v[224:227], v[102:105]
	v_mfma_f32_16x16x32_bf16 v[94:97], v[188:191], v[224:227], v[94:97]
	v_mfma_f32_16x16x32_bf16 v[86:89], v[172:175], v[232:235], v[86:89]
	v_mfma_f32_16x16x32_bf16 v[78:81], v[188:191], v[232:235], v[78:81]
	v_mfma_f32_16x16x32_bf16 v[114:117], v[184:187], v[204:207], v[114:117]
	v_mfma_f32_16x16x32_bf16 v[106:109], v[196:199], v[204:207], v[106:109]
	v_mfma_f32_16x16x32_bf16 v[98:101], v[184:187], v[212:215], v[98:101]
	v_mfma_f32_16x16x32_bf16 v[90:93], v[196:199], v[212:215], v[90:93]
	v_mfma_f32_16x16x32_bf16 v[82:85], v[184:187], v[220:223], v[82:85]
	v_mfma_f32_16x16x32_bf16 v[74:77], v[196:199], v[220:223], v[74:77]
	v_mfma_f32_16x16x32_bf16 v[70:73], v[184:187], v[228:231], v[70:73]
	v_mfma_f32_16x16x32_bf16 v[66:69], v[196:199], v[228:231], v[66:69]
	v_mfma_f32_16x16x32_bf16 v[114:117], v[192:195], v[208:211], v[114:117]
	v_mfma_f32_16x16x32_bf16 v[106:109], v[200:203], v[208:211], v[106:109]
	v_mfma_f32_16x16x32_bf16 v[98:101], v[192:195], v[216:219], v[98:101]
	v_mfma_f32_16x16x32_bf16 v[90:93], v[200:203], v[216:219], v[90:93]
	v_mfma_f32_16x16x32_bf16 v[82:85], v[192:195], v[224:227], v[82:85]
	v_mfma_f32_16x16x32_bf16 v[74:77], v[200:203], v[224:227], v[74:77]
	v_mfma_f32_16x16x32_bf16 v[70:73], v[192:195], v[232:235], v[70:73]
	v_mfma_f32_16x16x32_bf16 v[66:69], v[200:203], v[232:235], v[66:69]
	s_setprio 0
	s_barrier
	s_mov_b32 m0, s42
	v_lshl_add_u64 v[150:151], s[36:37], 0, v[130:131]
	s_add_u32 s76, s36, 0x80000
	ds_read_b128 v[204:207], v170 offset:16384
	ds_read_b128 v[208:211], v170 offset:17408
	ds_read_b128 v[212:215], v170 offset:18432
	ds_read_b128 v[216:219], v170 offset:19456
	ds_read_b128 v[220:223], v170 offset:20480
	ds_read_b128 v[224:227], v170 offset:21504
	ds_read_b128 v[228:231], v170 offset:22528
	ds_read_b128 v[232:235], v170 offset:23552
	global_load_lds_dwordx4 v[150:151], off
	v_lshl_add_u64 v[236:237], s[36:37], 0, v[136:137]
	s_mov_b32 m0, s43
	s_addc_u32 s77, s37, 0
	global_load_lds_dwordx4 v[236:237], off
	v_lshl_add_u64 v[238:239], s[76:77], 0, v[130:131]
	s_mov_b32 m0, s44
	v_lshl_add_u64 v[240:241], s[38:39], 0, v[138:139]
	global_load_lds_dwordx4 v[238:239], off
	v_lshl_add_u64 v[238:239], s[76:77], 0, v[136:137]
	s_mov_b32 m0, s45
	s_nop 0
	global_load_lds_dwordx4 v[238:239], off
	v_lshl_add_u64 v[238:239], s[38:39], 0, v[132:133]
	s_mov_b32 m0, s31
	s_nop 0
	global_load_lds_dwordx4 v[238:239], off
	s_mov_b32 m0, s46
	s_nop 0
	global_load_lds_dwordx4 v[240:241], off
	s_waitcnt vmcnt(8)
	s_waitcnt lgkmcnt(0)
	s_barrier
	s_setprio 1
	s_waitcnt lgkmcnt(0)
	v_mfma_f32_16x16x32_bf16 v[62:65], v[180:183], v[204:207], v[62:65]
	v_mfma_f32_16x16x32_bf16 v[58:61], v[176:179], v[204:207], v[58:61]
	v_mfma_f32_16x16x32_bf16 v[46:49], v[180:183], v[212:215], v[46:49]
	v_mfma_f32_16x16x32_bf16 v[38:41], v[176:179], v[212:215], v[38:41]
	v_mfma_f32_16x16x32_bf16 v[22:25], v[180:183], v[220:223], v[22:25]
	v_mfma_f32_16x16x32_bf16 v[14:17], v[176:179], v[220:223], v[14:17]
	v_mfma_f32_16x16x32_bf16 v[6:9], v[180:183], v[228:231], v[6:9]
	v_mfma_f32_16x16x32_bf16 v[2:5], v[176:179], v[228:231], v[2:5]
	v_mfma_f32_16x16x32_bf16 v[62:65], v[172:175], v[208:211], v[62:65]
	v_mfma_f32_16x16x32_bf16 v[58:61], v[188:191], v[208:211], v[58:61]
	v_mfma_f32_16x16x32_bf16 v[46:49], v[172:175], v[216:219], v[46:49]
	v_mfma_f32_16x16x32_bf16 v[38:41], v[188:191], v[216:219], v[38:41]
	v_mfma_f32_16x16x32_bf16 v[22:25], v[172:175], v[224:227], v[22:25]
	v_mfma_f32_16x16x32_bf16 v[14:17], v[188:191], v[224:227], v[14:17]
	v_mfma_f32_16x16x32_bf16 v[6:9], v[172:175], v[232:235], v[6:9]
	v_mfma_f32_16x16x32_bf16 v[2:5], v[188:191], v[232:235], v[2:5]
	v_mfma_f32_16x16x32_bf16 v[42:45], v[184:187], v[204:207], v[42:45]
	v_mfma_f32_16x16x32_bf16 v[30:33], v[196:199], v[204:207], v[30:33]
	v_mfma_f32_16x16x32_bf16 v[18:21], v[184:187], v[212:215], v[18:21]
	v_mfma_f32_16x16x32_bf16 v[10:13], v[196:199], v[212:215], v[10:13]
	v_mfma_f32_16x16x32_bf16 v[54:57], v[184:187], v[220:223], v[54:57]
	v_mfma_f32_16x16x32_bf16 v[50:53], v[196:199], v[220:223], v[50:53]
	v_mfma_f32_16x16x32_bf16 v[34:37], v[184:187], v[228:231], v[34:37]
	v_mfma_f32_16x16x32_bf16 v[26:29], v[196:199], v[228:231], v[26:29]
	v_mfma_f32_16x16x32_bf16 v[42:45], v[192:195], v[208:211], v[42:45]
	v_mfma_f32_16x16x32_bf16 v[30:33], v[200:203], v[208:211], v[30:33]
	v_mfma_f32_16x16x32_bf16 v[18:21], v[192:195], v[216:219], v[18:21]
	v_mfma_f32_16x16x32_bf16 v[10:13], v[200:203], v[216:219], v[10:13]
	v_mfma_f32_16x16x32_bf16 v[54:57], v[192:195], v[224:227], v[54:57]
	v_mfma_f32_16x16x32_bf16 v[50:53], v[200:203], v[224:227], v[50:53]
	v_mfma_f32_16x16x32_bf16 v[34:37], v[192:195], v[232:235], v[34:37]
	v_mfma_f32_16x16x32_bf16 v[26:29], v[200:203], v[232:235], v[26:29]
	s_setprio 0
	s_barrier
	ds_read_b128 v[172:175], v163
	ds_read_b128 v[176:179], v164
	ds_read_b128 v[180:183], v154
	ds_read_b128 v[184:187], v155
	ds_read_b128 v[188:191], v165
	ds_read_b128 v[192:195], v166
	ds_read_b128 v[196:199], v167
	ds_read_b128 v[200:203], v168
	s_mov_b32 m0, s47
	v_lshl_add_u64 v[242:243], s[38:39], 0, v[134:135]
	ds_read_b128 v[204:207], v170 offset:32768
	ds_read_b128 v[208:211], v170 offset:33792
	ds_read_b128 v[212:215], v170 offset:34816
	ds_read_b128 v[216:219], v170 offset:35840
	ds_read_b128 v[220:223], v170 offset:36864
	ds_read_b128 v[224:227], v170 offset:37888
	ds_read_b128 v[228:231], v170 offset:38912
	ds_read_b128 v[232:235], v170 offset:39936
	global_load_lds_dwordx4 v[242:243], off
	v_lshl_add_u64 v[242:243], s[38:39], 0, v[140:141]
	s_mov_b32 m0, s53
	s_nop 0
	global_load_lds_dwordx4 v[242:243], off
	s_waitcnt vmcnt(8)
	s_waitcnt lgkmcnt(0)
	s_barrier
	s_setprio 1
	s_waitcnt lgkmcnt(0)
	v_mfma_f32_16x16x32_bf16 v[126:129], v[180:183], v[204:207], v[126:129]
	v_mfma_f32_16x16x32_bf16 v[122:125], v[176:179], v[204:207], v[122:125]
	v_mfma_f32_16x16x32_bf16 v[118:121], v[180:183], v[212:215], v[118:121]
	v_mfma_f32_16x16x32_bf16 v[110:113], v[176:179], v[212:215], v[110:113]
	v_mfma_f32_16x16x32_bf16 v[102:105], v[180:183], v[220:223], v[102:105]
	v_mfma_f32_16x16x32_bf16 v[94:97], v[176:179], v[220:223], v[94:97]
	v_mfma_f32_16x16x32_bf16 v[86:89], v[180:183], v[228:231], v[86:89]
	v_mfma_f32_16x16x32_bf16 v[78:81], v[176:179], v[228:231], v[78:81]
	v_mfma_f32_16x16x32_bf16 v[126:129], v[172:175], v[208:211], v[126:129]
	v_mfma_f32_16x16x32_bf16 v[122:125], v[188:191], v[208:211], v[122:125]
	v_mfma_f32_16x16x32_bf16 v[118:121], v[172:175], v[216:219], v[118:121]
	v_mfma_f32_16x16x32_bf16 v[110:113], v[188:191], v[216:219], v[110:113]
	v_mfma_f32_16x16x32_bf16 v[102:105], v[172:175], v[224:227], v[102:105]
	v_mfma_f32_16x16x32_bf16 v[94:97], v[188:191], v[224:227], v[94:97]
	v_mfma_f32_16x16x32_bf16 v[86:89], v[172:175], v[232:235], v[86:89]
	v_mfma_f32_16x16x32_bf16 v[78:81], v[188:191], v[232:235], v[78:81]
	v_mfma_f32_16x16x32_bf16 v[114:117], v[184:187], v[204:207], v[114:117]
	v_mfma_f32_16x16x32_bf16 v[106:109], v[196:199], v[204:207], v[106:109]
	v_mfma_f32_16x16x32_bf16 v[98:101], v[184:187], v[212:215], v[98:101]
	v_mfma_f32_16x16x32_bf16 v[90:93], v[196:199], v[212:215], v[90:93]
	v_mfma_f32_16x16x32_bf16 v[82:85], v[184:187], v[220:223], v[82:85]
	v_mfma_f32_16x16x32_bf16 v[74:77], v[196:199], v[220:223], v[74:77]
	v_mfma_f32_16x16x32_bf16 v[70:73], v[184:187], v[228:231], v[70:73]
	v_mfma_f32_16x16x32_bf16 v[66:69], v[196:199], v[228:231], v[66:69]
	v_mfma_f32_16x16x32_bf16 v[114:117], v[192:195], v[208:211], v[114:117]
	v_mfma_f32_16x16x32_bf16 v[106:109], v[200:203], v[208:211], v[106:109]
	v_mfma_f32_16x16x32_bf16 v[98:101], v[192:195], v[216:219], v[98:101]
	v_mfma_f32_16x16x32_bf16 v[90:93], v[200:203], v[216:219], v[90:93]
	v_mfma_f32_16x16x32_bf16 v[82:85], v[192:195], v[224:227], v[82:85]
	v_mfma_f32_16x16x32_bf16 v[74:77], v[200:203], v[224:227], v[74:77]
	v_mfma_f32_16x16x32_bf16 v[70:73], v[192:195], v[232:235], v[70:73]
	v_mfma_f32_16x16x32_bf16 v[66:69], v[200:203], v[232:235], v[66:69]
	s_setprio 0
	s_barrier
	s_mov_b32 m0, s59
	v_lshl_add_u64 v[150:151], v[150:151], 0, s[12:13]
	s_add_u32 s36, s36, 0x80080
	ds_read_b128 v[204:207], v170 offset:49152
	ds_read_b128 v[208:211], v170 offset:50176
	ds_read_b128 v[212:215], v170 offset:51200
	ds_read_b128 v[216:219], v170 offset:52224
	ds_read_b128 v[220:223], v170 offset:53248
	ds_read_b128 v[224:227], v170 offset:54272
	ds_read_b128 v[228:231], v170 offset:55296
	ds_read_b128 v[232:235], v170 offset:56320
	global_load_lds_dwordx4 v[150:151], off
	v_lshl_add_u64 v[150:151], v[236:237], 0, s[12:13]
	s_mov_b32 m0, s60
	s_addc_u32 s37, s37, 0
	global_load_lds_dwordx4 v[150:151], off
	v_lshl_add_u64 v[150:151], s[36:37], 0, v[130:131]
	s_mov_b32 m0, s63
	s_nop 0
	global_load_lds_dwordx4 v[150:151], off
	v_lshl_add_u64 v[150:151], s[36:37], 0, v[136:137]
	s_mov_b32 m0, s64
	s_nop 0
	global_load_lds_dwordx4 v[150:151], off
	v_lshl_add_u64 v[150:151], v[238:239], 0, s[12:13]
	s_mov_b32 m0, s61
	s_nop 0
	global_load_lds_dwordx4 v[150:151], off
	v_lshl_add_u64 v[150:151], v[240:241], 0, s[12:13]
	s_mov_b32 m0, s62
	s_nop 0
	global_load_lds_dwordx4 v[150:151], off
	s_waitcnt vmcnt(8)
	s_waitcnt lgkmcnt(0)
	s_barrier
	s_setprio 1
	s_waitcnt lgkmcnt(0)
	v_mfma_f32_16x16x32_bf16 v[62:65], v[180:183], v[204:207], v[62:65]
	v_mfma_f32_16x16x32_bf16 v[58:61], v[176:179], v[204:207], v[58:61]
	v_mfma_f32_16x16x32_bf16 v[46:49], v[180:183], v[212:215], v[46:49]
	v_mfma_f32_16x16x32_bf16 v[38:41], v[176:179], v[212:215], v[38:41]
	v_mfma_f32_16x16x32_bf16 v[22:25], v[180:183], v[220:223], v[22:25]
	v_mfma_f32_16x16x32_bf16 v[14:17], v[176:179], v[220:223], v[14:17]
	v_mfma_f32_16x16x32_bf16 v[6:9], v[180:183], v[228:231], v[6:9]
	v_mfma_f32_16x16x32_bf16 v[2:5], v[176:179], v[228:231], v[2:5]
	v_mfma_f32_16x16x32_bf16 v[62:65], v[172:175], v[208:211], v[62:65]
	v_mfma_f32_16x16x32_bf16 v[58:61], v[188:191], v[208:211], v[58:61]
	v_mfma_f32_16x16x32_bf16 v[46:49], v[172:175], v[216:219], v[46:49]
	v_mfma_f32_16x16x32_bf16 v[38:41], v[188:191], v[216:219], v[38:41]
	v_mfma_f32_16x16x32_bf16 v[22:25], v[172:175], v[224:227], v[22:25]
	v_mfma_f32_16x16x32_bf16 v[14:17], v[188:191], v[224:227], v[14:17]
	v_mfma_f32_16x16x32_bf16 v[6:9], v[172:175], v[232:235], v[6:9]
	v_mfma_f32_16x16x32_bf16 v[2:5], v[188:191], v[232:235], v[2:5]
	v_mfma_f32_16x16x32_bf16 v[42:45], v[184:187], v[204:207], v[42:45]
	v_mfma_f32_16x16x32_bf16 v[30:33], v[196:199], v[204:207], v[30:33]
	v_mfma_f32_16x16x32_bf16 v[18:21], v[184:187], v[212:215], v[18:21]
	v_mfma_f32_16x16x32_bf16 v[10:13], v[196:199], v[212:215], v[10:13]
	v_mfma_f32_16x16x32_bf16 v[54:57], v[184:187], v[220:223], v[54:57]
	v_mfma_f32_16x16x32_bf16 v[50:53], v[196:199], v[220:223], v[50:53]
	v_mfma_f32_16x16x32_bf16 v[34:37], v[184:187], v[228:231], v[34:37]
	v_mfma_f32_16x16x32_bf16 v[26:29], v[196:199], v[228:231], v[26:29]
	v_mfma_f32_16x16x32_bf16 v[42:45], v[192:195], v[208:211], v[42:45]
	v_mfma_f32_16x16x32_bf16 v[30:33], v[200:203], v[208:211], v[30:33]
	v_mfma_f32_16x16x32_bf16 v[18:21], v[192:195], v[216:219], v[18:21]
	v_mfma_f32_16x16x32_bf16 v[10:13], v[200:203], v[216:219], v[10:13]
	v_mfma_f32_16x16x32_bf16 v[54:57], v[192:195], v[224:227], v[54:57]
	v_mfma_f32_16x16x32_bf16 v[50:53], v[200:203], v[224:227], v[50:53]
	v_mfma_f32_16x16x32_bf16 v[34:37], v[192:195], v[232:235], v[34:37]
	v_mfma_f32_16x16x32_bf16 v[26:29], v[200:203], v[232:235], v[26:29]
	s_setprio 0
	s_barrier
	s_add_i32 s74, s74, 2
	s_add_u32 s34, s34, 0x100
	s_addc_u32 s35, s35, 0
	s_add_u32 s72, s72, 0x100
	s_addc_u32 s73, s73, 0
	s_cmp_gt_u32 s74, 29
	s_cbranch_scc0 .LBB0_534
	s_and_b64 vcc, exec, s[14:15]
	s_cbranch_vccz .LBB0_537
	s_barrier

.LBB0_727:
	ds_read_b128 v[18:21], v192
	ds_read_b128 v[22:25], v193
	ds_read_b128 v[26:29], v194
	ds_read_b128 v[30:33], v195
	ds_read_b128 v[2:5], v196
	ds_read_b128 v[6:9], v197
	ds_read_b128 v[10:13], v198
	ds_read_b128 v[14:17], v199
	s_add_u32 s42, s16, s40
	s_addc_u32 s43, s17, s41
	s_add_u32 s44, s42, 0x2600100
	s_addc_u32 s45, s43, 0
	s_add_u32 s82, s31, s40
	s_addc_u32 s83, s35, s41
	s_cmpk_eq_i32 s40, 0x700
	s_cselect_b64 vcc, -1, 0
	s_and_b64 s[42:43], vcc, exec
	v_cndmask_b32_e32 v168, v215, v214, vcc
	s_cselect_b32 s45, s19, s45
	s_cselect_b32 s44, s18, s44
	v_cndmask_b32_e32 v184, v170, v213, vcc
	v_cndmask_b32_e32 v173, v172, v212, vcc
	v_cndmask_b32_e32 v175, v174, v211, vcc
	s_cselect_b32 s43, s37, s83
	s_cselect_b32 s42, s36, s82
	v_lshl_add_u64 v[180:181], v[178:179], 0, s[40:41]
	s_add_i32 m0, s59, 0xc000
	ds_read_b128 v[216:219], v209
	ds_read_b128 v[220:223], v209 offset:1024
	ds_read_b128 v[224:227], v209 offset:2048
	ds_read_b128 v[228:231], v209 offset:3072
	ds_read_b128 v[232:235], v209 offset:4096
	ds_read_b128 v[236:239], v209 offset:5120
	ds_read_b128 v[240:243], v209 offset:6144
	ds_read_b128 v[244:247], v209 offset:7168
	global_load_lds_dwordx4 v[180:181], off
	v_lshl_add_u64 v[180:181], v[176:177], 0, s[40:41]
	s_add_i32 m0, s59, 0xe000
	s_nop 0
	global_load_lds_dwordx4 v[180:181], off
	s_waitcnt vmcnt(8)
	s_waitcnt lgkmcnt(0)
	s_barrier
	s_setprio 1
	s_waitcnt lgkmcnt(0)
	v_mfma_f32_16x16x128_f8f6f4 v[158:161], v[18:25], v[216:223], v[158:161]
	v_mfma_f32_16x16x128_f8f6f4 v[150:153], v[26:33], v[216:223], v[150:153]
	v_mfma_f32_16x16x128_f8f6f4 v[142:145], v[18:25], v[224:231], v[142:145]
	v_mfma_f32_16x16x128_f8f6f4 v[134:137], v[26:33], v[224:231], v[134:137]
	v_mfma_f32_16x16x128_f8f6f4 v[126:129], v[18:25], v[232:239], v[126:129]
	v_mfma_f32_16x16x128_f8f6f4 v[118:121], v[26:33], v[232:239], v[118:121]
	v_mfma_f32_16x16x128_f8f6f4 v[110:113], v[18:25], v[240:247], v[110:113]
	v_mfma_f32_16x16x128_f8f6f4 v[102:105], v[26:33], v[240:247], v[102:105]
	v_mfma_f32_16x16x128_f8f6f4 v[154:157], v[2:9], v[216:223], v[154:157]
	v_mfma_f32_16x16x128_f8f6f4 v[146:149], v[10:17], v[216:223], v[146:149]
	v_mfma_f32_16x16x128_f8f6f4 v[138:141], v[2:9], v[224:231], v[138:141]
	v_mfma_f32_16x16x128_f8f6f4 v[130:133], v[10:17], v[224:231], v[130:133]
	v_mfma_f32_16x16x128_f8f6f4 v[122:125], v[2:9], v[232:239], v[122:125]
	v_mfma_f32_16x16x128_f8f6f4 v[114:117], v[10:17], v[232:239], v[114:117]
	v_mfma_f32_16x16x128_f8f6f4 v[106:109], v[2:9], v[240:247], v[106:109]
	v_mfma_f32_16x16x128_f8f6f4 v[98:101], v[10:17], v[240:247], v[98:101]
	s_setprio 0
	s_barrier
	s_mov_b32 m0, s60
	v_lshl_add_u64 v[180:181], s[42:43], 0, v[166:167]
	s_add_u32 s82, s42, 0x40000
	ds_read_b128 v[216:219], v209 offset:16384
	ds_read_b128 v[220:223], v209 offset:17408
	ds_read_b128 v[224:227], v209 offset:18432
	ds_read_b128 v[228:231], v209 offset:19456
	ds_read_b128 v[232:235], v209 offset:20480
	ds_read_b128 v[236:239], v209 offset:21504
	ds_read_b128 v[240:243], v209 offset:22528
	ds_read_b128 v[244:247], v209 offset:23552
	global_load_lds_dwordx4 v[180:181], off
	v_lshl_add_u64 v[182:183], s[42:43], 0, v[164:165]
	s_mov_b32 m0, s61
	s_addc_u32 s83, s43, 0
	global_load_lds_dwordx4 v[182:183], off
	v_lshl_add_u64 v[186:187], s[82:83], 0, v[166:167]
	s_mov_b32 m0, s62
	v_mov_b32_e32 v185, v169
	global_load_lds_dwordx4 v[186:187], off
	v_lshl_add_u64 v[186:187], s[82:83], 0, v[164:165]
	s_mov_b32 m0, s63
	s_nop 0
	global_load_lds_dwordx4 v[186:187], off
	s_mov_b32 m0, s59
	v_lshl_add_u64 v[186:187], s[44:45], 0, v[168:169]
	global_load_lds_dwordx4 v168, s[44:45]
	s_mov_b32 m0, s64
	s_nop 0
	global_load_lds_dwordx4 v184, s[44:45]
	s_waitcnt vmcnt(8)
	s_waitcnt lgkmcnt(0)
	v_lshl_add_u64 v[184:185], s[44:45], 0, v[184:185]
	s_barrier
	s_setprio 1
	s_waitcnt lgkmcnt(0)
	v_mfma_f32_16x16x128_f8f6f4 v[94:97], v[18:25], v[216:223], v[94:97]
	v_mfma_f32_16x16x128_f8f6f4 v[86:89], v[26:33], v[216:223], v[86:89]
	v_mfma_f32_16x16x128_f8f6f4 v[78:81], v[18:25], v[224:231], v[78:81]
	v_mfma_f32_16x16x128_f8f6f4 v[70:73], v[26:33], v[224:231], v[70:73]
	v_mfma_f32_16x16x128_f8f6f4 v[62:65], v[18:25], v[232:239], v[62:65]
	v_mfma_f32_16x16x128_f8f6f4 v[54:57], v[26:33], v[232:239], v[54:57]
	v_mfma_f32_16x16x128_f8f6f4 v[46:49], v[18:25], v[240:247], v[46:49]
	v_mfma_f32_16x16x128_f8f6f4 v[38:41], v[26:33], v[240:247], v[38:41]
	v_mfma_f32_16x16x128_f8f6f4 v[90:93], v[2:9], v[216:223], v[90:93]
	v_mfma_f32_16x16x128_f8f6f4 v[82:85], v[10:17], v[216:223], v[82:85]
	v_mfma_f32_16x16x128_f8f6f4 v[74:77], v[2:9], v[224:231], v[74:77]
	v_mfma_f32_16x16x128_f8f6f4 v[66:69], v[10:17], v[224:231], v[66:69]
	v_mfma_f32_16x16x128_f8f6f4 v[58:61], v[2:9], v[232:239], v[58:61]
	v_mfma_f32_16x16x128_f8f6f4 v[50:53], v[10:17], v[232:239], v[50:53]
	v_mfma_f32_16x16x128_f8f6f4 v[42:45], v[2:9], v[240:247], v[42:45]
	v_mfma_f32_16x16x128_f8f6f4 v[34:37], v[10:17], v[240:247], v[34:37]
	s_setprio 0
	s_barrier
	ds_read_b128 v[2:5], v200
	ds_read_b128 v[6:9], v201
	ds_read_b128 v[10:13], v202
	ds_read_b128 v[14:17], v203
	ds_read_b128 v[18:21], v204
	ds_read_b128 v[22:25], v205
	ds_read_b128 v[26:29], v206
	ds_read_b128 v[30:33], v207
	s_mov_b32 m0, s65
	ds_read_b128 v[216:219], v209 offset:32768
	ds_read_b128 v[220:223], v209 offset:33792
	ds_read_b128 v[224:227], v209 offset:34816
	ds_read_b128 v[228:231], v209 offset:35840
	ds_read_b128 v[232:235], v209 offset:36864
	ds_read_b128 v[236:239], v209 offset:37888
	ds_read_b128 v[240:243], v209 offset:38912
	ds_read_b128 v[244:247], v209 offset:39936
	global_load_lds_dwordx4 v173, s[44:45]
	s_mov_b32 m0, s66
	s_nop 0
	global_load_lds_dwordx4 v175, s[44:45]
	s_waitcnt vmcnt(8)
	s_waitcnt lgkmcnt(0)
	s_barrier
	s_setprio 1
	s_waitcnt lgkmcnt(0)
	v_mfma_f32_16x16x128_f8f6f4 v[158:161], v[2:9], v[216:223], v[158:161]
	v_mfma_f32_16x16x128_f8f6f4 v[150:153], v[10:17], v[216:223], v[150:153]
	v_mfma_f32_16x16x128_f8f6f4 v[142:145], v[2:9], v[224:231], v[142:145]
	v_mfma_f32_16x16x128_f8f6f4 v[134:137], v[10:17], v[224:231], v[134:137]
	v_mfma_f32_16x16x128_f8f6f4 v[126:129], v[2:9], v[232:239], v[126:129]
	v_mfma_f32_16x16x128_f8f6f4 v[118:121], v[10:17], v[232:239], v[118:121]
	v_mfma_f32_16x16x128_f8f6f4 v[110:113], v[2:9], v[240:247], v[110:113]
	v_mfma_f32_16x16x128_f8f6f4 v[102:105], v[10:17], v[240:247], v[102:105]
	v_mfma_f32_16x16x128_f8f6f4 v[154:157], v[18:25], v[216:223], v[154:157]
	v_mfma_f32_16x16x128_f8f6f4 v[146:149], v[26:33], v[216:223], v[146:149]
	v_mfma_f32_16x16x128_f8f6f4 v[138:141], v[18:25], v[224:231], v[138:141]
	v_mfma_f32_16x16x128_f8f6f4 v[130:133], v[26:33], v[224:231], v[130:133]
	v_mfma_f32_16x16x128_f8f6f4 v[122:125], v[18:25], v[232:239], v[122:125]
	v_mfma_f32_16x16x128_f8f6f4 v[114:117], v[26:33], v[232:239], v[114:117]
	v_mfma_f32_16x16x128_f8f6f4 v[106:109], v[18:25], v[240:247], v[106:109]
	v_mfma_f32_16x16x128_f8f6f4 v[98:101], v[26:33], v[240:247], v[98:101]
	s_setprio 0
	s_barrier
	s_mov_b32 m0, s67
	v_lshl_add_u64 v[180:181], v[180:181], 0, s[24:25]
	s_add_u32 s42, s42, 0x40080
	ds_read_b128 v[216:219], v209 offset:49152
	ds_read_b128 v[220:223], v209 offset:50176
	ds_read_b128 v[224:227], v209 offset:51200
	ds_read_b128 v[228:231], v209 offset:52224
	ds_read_b128 v[232:235], v209 offset:53248
	ds_read_b128 v[236:239], v209 offset:54272
	ds_read_b128 v[240:243], v209 offset:55296
	ds_read_b128 v[244:247], v209 offset:56320
	global_load_lds_dwordx4 v[180:181], off
	v_lshl_add_u64 v[180:181], v[182:183], 0, s[24:25]
	s_mov_b32 m0, s68
	s_addc_u32 s43, s43, 0
	global_load_lds_dwordx4 v[180:181], off
	v_lshl_add_u64 v[180:181], s[42:43], 0, v[166:167]
	s_mov_b32 m0, s71
	s_nop 0
	global_load_lds_dwordx4 v[180:181], off
	v_lshl_add_u64 v[180:181], s[42:43], 0, v[164:165]
	s_mov_b32 m0, s72
	s_nop 0
	global_load_lds_dwordx4 v[180:181], off
	v_lshl_add_u64 v[180:181], v[186:187], 0, s[24:25]
	s_mov_b32 m0, s69
	s_nop 0
	global_load_lds_dwordx4 v[180:181], off
	v_lshl_add_u64 v[180:181], v[184:185], 0, s[24:25]
	s_mov_b32 m0, s70
	s_nop 0
	global_load_lds_dwordx4 v[180:181], off
	s_waitcnt vmcnt(8)
	s_waitcnt lgkmcnt(0)
	s_barrier
	s_setprio 1
	s_waitcnt lgkmcnt(0)
	v_mfma_f32_16x16x128_f8f6f4 v[94:97], v[2:9], v[216:223], v[94:97]
	v_mfma_f32_16x16x128_f8f6f4 v[86:89], v[10:17], v[216:223], v[86:89]
	v_mfma_f32_16x16x128_f8f6f4 v[78:81], v[2:9], v[224:231], v[78:81]
	v_mfma_f32_16x16x128_f8f6f4 v[70:73], v[10:17], v[224:231], v[70:73]
	v_mfma_f32_16x16x128_f8f6f4 v[62:65], v[2:9], v[232:239], v[62:65]
	v_mfma_f32_16x16x128_f8f6f4 v[54:57], v[10:17], v[232:239], v[54:57]
	v_mfma_f32_16x16x128_f8f6f4 v[46:49], v[2:9], v[240:247], v[46:49]
	v_mfma_f32_16x16x128_f8f6f4 v[38:41], v[10:17], v[240:247], v[38:41]
	v_mfma_f32_16x16x128_f8f6f4 v[90:93], v[18:25], v[216:223], v[90:93]
	v_mfma_f32_16x16x128_f8f6f4 v[82:85], v[26:33], v[216:223], v[82:85]
	v_mfma_f32_16x16x128_f8f6f4 v[74:77], v[18:25], v[224:231], v[74:77]
	v_mfma_f32_16x16x128_f8f6f4 v[66:69], v[26:33], v[224:231], v[66:69]
	v_mfma_f32_16x16x128_f8f6f4 v[58:61], v[18:25], v[232:239], v[58:61]
	v_mfma_f32_16x16x128_f8f6f4 v[50:53], v[26:33], v[232:239], v[50:53]
	v_mfma_f32_16x16x128_f8f6f4 v[42:45], v[18:25], v[240:247], v[42:45]
	v_mfma_f32_16x16x128_f8f6f4 v[34:37], v[26:33], v[240:247], v[34:37]
	s_setprio 0
	s_barrier
	s_add_i32 s81, s81, 2
	s_add_u32 s40, s40, 0x100
	s_addc_u32 s41, s41, 0
	s_cmp_gt_u32 s81, 13
	s_cbranch_scc0 .LBB0_727
	s_and_b64 vcc, exec, s[28:29]
	s_cbranch_vccz .LBB0_730
	s_barrier

.LBB0_831:
	ds_read_b128 v[18:21], v188
	ds_read_b128 v[22:25], v189
	ds_read_b128 v[26:29], v190
	ds_read_b128 v[30:33], v191
	ds_read_b128 v[2:5], v192
	ds_read_b128 v[6:9], v193
	ds_read_b128 v[10:13], v194
	ds_read_b128 v[14:17], v195
	s_add_u32 s64, s62, 0x80
	s_addc_u32 s65, s63, 0
	s_cmp_eq_u32 s91, 12
	s_cselect_b32 s67, s17, s65
	s_cselect_b32 s66, s39, s64
	s_cselect_b32 s65, s43, s90
	s_cselect_b32 s64, s42, s41
	v_lshl_add_u64 v[232:233], s[62:63], 0, v[176:177]
	s_add_i32 m0, s61, 0xc000
	ds_read_b128 v[180:183], v206
	ds_read_b128 v[184:187], v206 offset:1024
	ds_read_b128 v[208:211], v206 offset:2048
	ds_read_b128 v[212:215], v206 offset:3072
	ds_read_b128 v[216:219], v206 offset:4096
	ds_read_b128 v[220:223], v206 offset:5120
	ds_read_b128 v[224:227], v206 offset:6144
	ds_read_b128 v[228:231], v206 offset:7168
	global_load_lds_dwordx4 v[232:233], off
	v_lshl_add_u64 v[232:233], s[62:63], 0, v[178:179]
	s_add_i32 m0, s61, 0xe000
	s_nop 0
	global_load_lds_dwordx4 v[232:233], off
	s_waitcnt vmcnt(8)
	s_waitcnt lgkmcnt(0)
	s_barrier
	s_setprio 1
	s_waitcnt lgkmcnt(0)
	v_mfma_f32_16x16x128_f8f6f4 v[158:161], v[18:25], v[180:187], v[158:161]
	v_mfma_f32_16x16x128_f8f6f4 v[154:157], v[26:33], v[180:187], v[154:157]
	v_mfma_f32_16x16x128_f8f6f4 v[146:149], v[18:25], v[208:215], v[146:149]
	v_mfma_f32_16x16x128_f8f6f4 v[138:141], v[26:33], v[208:215], v[138:141]
	v_mfma_f32_16x16x128_f8f6f4 v[130:133], v[18:25], v[216:223], v[130:133]
	v_mfma_f32_16x16x128_f8f6f4 v[122:125], v[26:33], v[216:223], v[122:125]
	v_mfma_f32_16x16x128_f8f6f4 v[114:117], v[18:25], v[224:231], v[114:117]
	v_mfma_f32_16x16x128_f8f6f4 v[106:109], v[26:33], v[224:231], v[106:109]
	v_mfma_f32_16x16x128_f8f6f4 v[150:153], v[2:9], v[180:187], v[150:153]
	v_mfma_f32_16x16x128_f8f6f4 v[142:145], v[10:17], v[180:187], v[142:145]
	v_mfma_f32_16x16x128_f8f6f4 v[134:137], v[2:9], v[208:215], v[134:137]
	v_mfma_f32_16x16x128_f8f6f4 v[126:129], v[10:17], v[208:215], v[126:129]
	v_mfma_f32_16x16x128_f8f6f4 v[118:121], v[2:9], v[216:223], v[118:121]
	v_mfma_f32_16x16x128_f8f6f4 v[110:113], v[10:17], v[216:223], v[110:113]
	v_mfma_f32_16x16x128_f8f6f4 v[102:105], v[2:9], v[224:231], v[102:105]
	v_mfma_f32_16x16x128_f8f6f4 v[98:101], v[10:17], v[224:231], v[98:101]
	s_setprio 0
	s_barrier
	s_mov_b32 m0, s68
	v_lshl_add_u64 v[180:181], s[64:65], 0, v[164:165]
	s_add_u32 s92, s64, 0x40000
	ds_read_b128 v[208:211], v206 offset:16384
	ds_read_b128 v[212:215], v206 offset:17408
	ds_read_b128 v[216:219], v206 offset:18432
	ds_read_b128 v[220:223], v206 offset:19456
	ds_read_b128 v[224:227], v206 offset:20480
	ds_read_b128 v[228:231], v206 offset:21504
	ds_read_b128 v[232:235], v206 offset:22528
	ds_read_b128 v[236:239], v206 offset:23552
	global_load_lds_dwordx4 v[180:181], off
	v_lshl_add_u64 v[182:183], s[64:65], 0, v[170:171]
	s_mov_b32 m0, s69
	s_addc_u32 s93, s65, 0
	global_load_lds_dwordx4 v[182:183], off
	v_lshl_add_u64 v[184:185], s[92:93], 0, v[164:165]
	s_mov_b32 m0, s70
	v_lshl_add_u64 v[186:187], s[66:67], 0, v[172:173]
	global_load_lds_dwordx4 v[184:185], off
	v_lshl_add_u64 v[184:185], s[92:93], 0, v[170:171]
	s_mov_b32 m0, s71
	s_nop 0
	global_load_lds_dwordx4 v[184:185], off
	v_lshl_add_u64 v[184:185], s[66:67], 0, v[166:167]
	s_mov_b32 m0, s61
	s_nop 0
	global_load_lds_dwordx4 v[184:185], off
	s_mov_b32 m0, s72
	s_nop 0
	global_load_lds_dwordx4 v[186:187], off
	s_waitcnt vmcnt(8)
	s_waitcnt lgkmcnt(0)
	s_barrier
	s_setprio 1
	s_waitcnt lgkmcnt(0)
	v_mfma_f32_16x16x128_f8f6f4 v[94:97], v[18:25], v[208:215], v[94:97]
	v_mfma_f32_16x16x128_f8f6f4 v[90:93], v[26:33], v[208:215], v[90:93]
	v_mfma_f32_16x16x128_f8f6f4 v[82:85], v[18:25], v[216:223], v[82:85]
	v_mfma_f32_16x16x128_f8f6f4 v[70:73], v[26:33], v[216:223], v[70:73]
	v_mfma_f32_16x16x128_f8f6f4 v[58:61], v[18:25], v[224:231], v[58:61]
	v_mfma_f32_16x16x128_f8f6f4 v[42:45], v[26:33], v[224:231], v[42:45]
	v_mfma_f32_16x16x128_f8f6f4 v[38:41], v[18:25], v[232:239], v[38:41]
	v_mfma_f32_16x16x128_f8f6f4 v[34:37], v[26:33], v[232:239], v[34:37]
	v_mfma_f32_16x16x128_f8f6f4 v[86:89], v[2:9], v[208:215], v[86:89]
	v_mfma_f32_16x16x128_f8f6f4 v[78:81], v[10:17], v[208:215], v[78:81]
	v_mfma_f32_16x16x128_f8f6f4 v[62:65], v[2:9], v[216:223], v[62:65]
	v_mfma_f32_16x16x128_f8f6f4 v[46:49], v[10:17], v[216:223], v[46:49]
	v_mfma_f32_16x16x128_f8f6f4 v[74:77], v[2:9], v[224:231], v[74:77]
	v_mfma_f32_16x16x128_f8f6f4 v[66:69], v[10:17], v[224:231], v[66:69]
	v_mfma_f32_16x16x128_f8f6f4 v[54:57], v[2:9], v[232:239], v[54:57]
	v_mfma_f32_16x16x128_f8f6f4 v[50:53], v[10:17], v[232:239], v[50:53]
	s_setprio 0
	s_barrier
	ds_read_b128 v[2:5], v196
	ds_read_b128 v[6:9], v197
	ds_read_b128 v[10:13], v198
	ds_read_b128 v[14:17], v199
	ds_read_b128 v[18:21], v200
	ds_read_b128 v[22:25], v201
	ds_read_b128 v[26:29], v202
	ds_read_b128 v[30:33], v203
	s_mov_b32 m0, s73
	v_lshl_add_u64 v[240:241], s[66:67], 0, v[168:169]
	ds_read_b128 v[208:211], v206 offset:32768
	ds_read_b128 v[212:215], v206 offset:33792
	ds_read_b128 v[216:219], v206 offset:34816
	ds_read_b128 v[220:223], v206 offset:35840
	ds_read_b128 v[224:227], v206 offset:36864
	ds_read_b128 v[228:231], v206 offset:37888
	ds_read_b128 v[232:235], v206 offset:38912
	ds_read_b128 v[236:239], v206 offset:39936
	global_load_lds_dwordx4 v[240:241], off
	v_lshl_add_u64 v[240:241], s[66:67], 0, v[174:175]
	s_mov_b32 m0, s74
	s_nop 0
	global_load_lds_dwordx4 v[240:241], off
	s_waitcnt vmcnt(8)
	s_waitcnt lgkmcnt(0)
	s_barrier
	s_setprio 1
	s_waitcnt lgkmcnt(0)
	v_mfma_f32_16x16x128_f8f6f4 v[158:161], v[2:9], v[208:215], v[158:161]
	v_mfma_f32_16x16x128_f8f6f4 v[154:157], v[10:17], v[208:215], v[154:157]
	v_mfma_f32_16x16x128_f8f6f4 v[146:149], v[2:9], v[216:223], v[146:149]
	v_mfma_f32_16x16x128_f8f6f4 v[138:141], v[10:17], v[216:223], v[138:141]
	v_mfma_f32_16x16x128_f8f6f4 v[130:133], v[2:9], v[224:231], v[130:133]
	v_mfma_f32_16x16x128_f8f6f4 v[122:125], v[10:17], v[224:231], v[122:125]
	v_mfma_f32_16x16x128_f8f6f4 v[114:117], v[2:9], v[232:239], v[114:117]
	v_mfma_f32_16x16x128_f8f6f4 v[106:109], v[10:17], v[232:239], v[106:109]
	v_mfma_f32_16x16x128_f8f6f4 v[150:153], v[18:25], v[208:215], v[150:153]
	v_mfma_f32_16x16x128_f8f6f4 v[142:145], v[26:33], v[208:215], v[142:145]
	v_mfma_f32_16x16x128_f8f6f4 v[134:137], v[18:25], v[216:223], v[134:137]
	v_mfma_f32_16x16x128_f8f6f4 v[126:129], v[26:33], v[216:223], v[126:129]
	v_mfma_f32_16x16x128_f8f6f4 v[118:121], v[18:25], v[224:231], v[118:121]
	v_mfma_f32_16x16x128_f8f6f4 v[110:113], v[26:33], v[224:231], v[110:113]
	v_mfma_f32_16x16x128_f8f6f4 v[102:105], v[18:25], v[232:239], v[102:105]
	v_mfma_f32_16x16x128_f8f6f4 v[98:101], v[26:33], v[232:239], v[98:101]
	s_setprio 0
	s_barrier
	s_mov_b32 m0, s79
	v_lshl_add_u64 v[180:181], v[180:181], 0, s[24:25]
	s_add_u32 s64, s64, 0x40080
	ds_read_b128 v[208:211], v206 offset:49152
	ds_read_b128 v[212:215], v206 offset:50176
	ds_read_b128 v[216:219], v206 offset:51200
	ds_read_b128 v[220:223], v206 offset:52224
	ds_read_b128 v[224:227], v206 offset:53248
	ds_read_b128 v[228:231], v206 offset:54272
	ds_read_b128 v[232:235], v206 offset:55296
	ds_read_b128 v[236:239], v206 offset:56320
	global_load_lds_dwordx4 v[180:181], off
	v_lshl_add_u64 v[180:181], v[182:183], 0, s[24:25]
	s_mov_b32 m0, s80
	s_addc_u32 s65, s65, 0
	global_load_lds_dwordx4 v[180:181], off
	v_lshl_add_u64 v[180:181], s[64:65], 0, v[164:165]
	s_mov_b32 m0, s83
	s_nop 0
	global_load_lds_dwordx4 v[180:181], off
	v_lshl_add_u64 v[180:181], s[64:65], 0, v[170:171]
	s_mov_b32 m0, s84
	s_nop 0
	global_load_lds_dwordx4 v[180:181], off
	v_lshl_add_u64 v[180:181], v[184:185], 0, s[24:25]
	s_mov_b32 m0, s81
	s_nop 0
	global_load_lds_dwordx4 v[180:181], off
	v_lshl_add_u64 v[180:181], v[186:187], 0, s[24:25]
	s_mov_b32 m0, s82
	s_nop 0
	global_load_lds_dwordx4 v[180:181], off
	s_waitcnt vmcnt(8)
	s_waitcnt lgkmcnt(0)
	s_barrier
	s_setprio 1
	s_waitcnt lgkmcnt(0)
	v_mfma_f32_16x16x128_f8f6f4 v[94:97], v[2:9], v[208:215], v[94:97]
	v_mfma_f32_16x16x128_f8f6f4 v[90:93], v[10:17], v[208:215], v[90:93]
	v_mfma_f32_16x16x128_f8f6f4 v[82:85], v[2:9], v[216:223], v[82:85]
	v_mfma_f32_16x16x128_f8f6f4 v[70:73], v[10:17], v[216:223], v[70:73]
	v_mfma_f32_16x16x128_f8f6f4 v[58:61], v[2:9], v[224:231], v[58:61]
	v_mfma_f32_16x16x128_f8f6f4 v[42:45], v[10:17], v[224:231], v[42:45]
	v_mfma_f32_16x16x128_f8f6f4 v[38:41], v[2:9], v[232:239], v[38:41]
	v_mfma_f32_16x16x128_f8f6f4 v[34:37], v[10:17], v[232:239], v[34:37]
	v_mfma_f32_16x16x128_f8f6f4 v[86:89], v[18:25], v[208:215], v[86:89]
	v_mfma_f32_16x16x128_f8f6f4 v[78:81], v[26:33], v[208:215], v[78:81]
	v_mfma_f32_16x16x128_f8f6f4 v[62:65], v[18:25], v[216:223], v[62:65]
	v_mfma_f32_16x16x128_f8f6f4 v[46:49], v[26:33], v[216:223], v[46:49]
	v_mfma_f32_16x16x128_f8f6f4 v[74:77], v[18:25], v[224:231], v[74:77]
	v_mfma_f32_16x16x128_f8f6f4 v[66:69], v[26:33], v[224:231], v[66:69]
	v_mfma_f32_16x16x128_f8f6f4 v[54:57], v[18:25], v[232:239], v[54:57]
	v_mfma_f32_16x16x128_f8f6f4 v[50:53], v[26:33], v[232:239], v[50:53]
	s_setprio 0
	s_barrier
	s_add_i32 s91, s91, 2
	s_add_u32 s62, s62, 0x100
	s_addc_u32 s63, s63, 0
	s_add_u32 s41, s41, 0x100
	s_addc_u32 s90, s90, 0
	s_cmp_gt_u32 s91, 13
	s_cbranch_scc0 .LBB0_831
	s_and_b64 vcc, exec, s[26:27]
	s_cbranch_vccz .LBB0_834
	s_barrier
